# c38: c37 + FINAL loop software-pipelined: the next pass's 28 loads are issued one pass ahead into spare VGPRs and copied at the pass head (counted vmcnt(8) for the 8 stores)
# baseline (speedup 1.0000x reference)
; #define GAS __attribute__((address_space(1)))
; __global__ void __launch_bounds__(NTHREADS, 2) fwd(Args args) {
;     ...
;     if (IN(PH_FINAL)) {
;         const GAS f32x4* gr = (const GAS f32x4*)args.in[6] + F.lane;
;         f32x4 gn[4];
; #pragma unroll
;         for (int q = 0; q < 4; ++q) gn[q] = gr[64 * q];
;         for (int t0 = 2 * gw; t0 < SEQ; t0 += 2 * NGW) {
;             unsigned long long hr[2][4]; unsigned pr[2][2][4]; int sl[2][2];
; #pragma unroll
;             for (int r = 0; r < 2; ++r) { const int t = t0 + r;
;                 const GAS unsigned long long* hp = (const GAS unsigned long long*)(HN + (size_t)t * DM) + F.lane;
; #pragma unroll
;                 for (int q = 0; q < 4; ++q) hr[r][q] = __builtin_nontemporal_load(hp + 64 * q);
; #pragma unroll
;                 for (int k = 0; k < 2; ++k) { const GAS unsigned* pa = (const GAS unsigned*)((const unsigned char*)PAIR + (size_t)(2 * t + k) * DM) + F.lane;
; #pragma unroll
;                     for (int q = 0; q < 4; ++q) pr[r][k][q] = __builtin_nontemporal_load(pa + 64 * q);
;                     sl[r][k] = SLOTOF[2 * t + k]; } }
.LBB0_1475:
	s_cmp_lt_i32 s64, 15
	s_cselect_b64 s[0:1], -1, 0
	s_and_b64 s[0:1], s[0:1], s[6:7]
	s_andn2_b64 vcc, exec, s[0:1]
	s_cbranch_vccnz .LBB0_1495
	s_cmpk_gt_i32 s66, 0x1fff
	s_cbranch_scc1 .LBB0_1495
	s_waitcnt vmcnt(0)
	v_lshlrev_b32_e32 v52, 4, v162
	global_load_dwordx4 v[0:3], v52, s[28:29]
	global_load_dwordx4 v[4:7], v52, s[28:29] offset:1024
	global_load_dwordx4 v[8:11], v52, s[28:29] offset:2048
	global_load_dwordx4 v[12:15], v52, s[28:29] offset:3072
	v_mbcnt_lo_u32_b32 v16, -1, 0
	v_mbcnt_hi_u32_b32 v16, -1, v16
	v_and_b32_e32 v17, 64, v16
	v_add_u32_e32 v17, 64, v17
	v_xor_b32_e32 v18, 1, v16
	v_cmp_lt_i32_e32 vcc, v18, v17
	s_lshl_b32 s0, s66, 1
	s_add_u32 s7, s34, 0x2b8000
	v_cndmask_b32_e32 v18, v16, v18, vcc
	v_lshlrev_b32_e32 v76, 2, v18
	v_xor_b32_e32 v18, 2, v16
	v_cmp_lt_i32_e32 vcc, v18, v17
	s_addc_u32 s20, s35, 0
	s_add_u32 s21, s34, 0x210000
	v_cndmask_b32_e32 v18, v16, v18, vcc
	v_lshlrev_b32_e32 v77, 2, v18
	v_xor_b32_e32 v18, 4, v16
	v_cmp_lt_i32_e32 vcc, v18, v17
	v_mov_b32_e32 v53, 0
	s_addc_u32 s22, s35, 0
	v_cndmask_b32_e32 v18, v16, v18, vcc
	v_lshlrev_b32_e32 v78, 2, v18
	v_xor_b32_e32 v18, 8, v16
	v_cmp_lt_i32_e32 vcc, v18, v17
	s_add_u32 s23, s34, 0x18400000
	s_addc_u32 s24, s35, 0
	v_cndmask_b32_e32 v18, v16, v18, vcc
	v_lshlrev_b32_e32 v79, 2, v18
	v_xor_b32_e32 v18, 16, v16
	v_cmp_lt_i32_e32 vcc, v18, v17
	s_mov_b64 s[4:5], 0x14400000
	s_ashr_i32 s1, s0, 31
	v_cndmask_b32_e32 v18, v16, v18, vcc
	v_lshlrev_b32_e32 v80, 2, v18
	v_xor_b32_e32 v18, 32, v16
	v_cmp_lt_i32_e32 vcc, v18, v17
	v_mov_b32_e32 v17, v53
	s_mov_b32 s3, 0
	v_cndmask_b32_e32 v16, v16, v18, vcc
	v_lshlrev_b32_e32 v81, 2, v16
	v_lshlrev_b32_e32 v16, 2, v162
	v_lshl_add_u64 v[16:17], s[34:35], 0, v[16:17]
	v_lshl_add_u64 v[54:55], v[16:17], 0, s[4:5]
	s_lshl_b64 s[4:5], s[0:1], 12
	s_add_u32 s4, s62, s4
	s_addc_u32 s5, s63, s5
	v_lshl_add_u64 v[16:17], s[4:5], 0, v[52:53]
	s_mov_b64 s[4:5], 0x1000
	v_lshl_add_u64 v[56:57], v[16:17], 0, s[4:5]
	s_lshl_b32 s4, s2, 4
	s_lshl_b32 s5, s82, 1
	s_add_i32 s4, s4, s5
	s_add_i32 s25, s4, 0xfffff000
	s_lshl_b64 s[0:1], s[0:1], 11
	s_add_u32 s0, s34, s0
	v_lshlrev_b32_e32 v52, 3, v162
	s_addc_u32 s1, s35, s1
	v_lshl_add_u64 v[16:17], s[0:1], 0, v[52:53]
	s_mov_b64 s[0:1], 0x2600000
	v_lshl_add_u64 v[58:59], v[16:17], 0, s[0:1]
	s_lshl_b32 s0, s2, 5
	s_lshl_b32 s1, s82, 2
	s_add_i32 s4, s0, s1
	s_mov_b32 s26, 0x40000
	s_mov_b32 s27, 0x80000
	s_mov_b32 s28, 0xc0000
	s_mov_b32 s29, 0x100000
	s_mov_b32 s30, 0x140000
	s_mov_b32 s31, 0x180000
	s_mov_b32 s6, 0x3d800000
	v_mov_b32_e32 v82, 0x3727c5ac
	s_mov_b32 s33, 0xf800000
	v_mov_b32_e32 v83, 0x260
	s_mov_b64 s[8:9], 0x1000000
	s_mov_b64 s[10:11], 0x800000
	s_mov_b32 s44, s4
	s_ashr_i32 s45, s44, 31
	s_lshl_b64 s[46:47], s[44:45], 10
	s_lshl_b64 s[44:45], s[44:45], 2
	s_add_u32 s44, s7, s44
	s_addc_u32 s45, s20, s45
	v_lshl_add_u64 v[228:229], v[54:55], 0, s[46:47]
	v_mov_b32_e32 v230, v58
	v_mov_b32_e32 v231, v59
	global_load_dwordx2 v[192:193], v[230:231], off nt
	global_load_dwordx2 v[194:195], v[230:231], off offset:512 nt
	global_load_dwordx2 v[196:197], v[230:231], off offset:1024 nt
	global_load_dwordx2 v[198:199], v[230:231], off offset:1536 nt
	global_load_dwordx2 v[200:201], v[230:231], off offset:2048 nt
	global_load_dwordx2 v[202:203], v[230:231], off offset:2560 nt
	global_load_dwordx2 v[204:205], v[230:231], off offset:3072 nt
	global_load_dwordx2 v[206:207], v[230:231], off offset:3584 nt
	global_load_dword v208, v[228:229], off nt
	global_load_dword v209, v[228:229], off offset:256 nt
	global_load_dword v210, v[228:229], off offset:512 nt
	global_load_dword v211, v[228:229], off offset:768 nt
	global_load_dword v212, v[228:229], off offset:1024 nt
	global_load_dword v213, v[228:229], off offset:1280 nt
	global_load_dword v214, v[228:229], off offset:1536 nt
	global_load_dword v215, v[228:229], off offset:1792 nt
	global_load_dword v216, v[228:229], off offset:2048 nt
	global_load_dword v217, v[228:229], off offset:2304 nt
	global_load_dword v218, v[228:229], off offset:2560 nt
	global_load_dword v219, v[228:229], off offset:2816 nt
	global_load_dword v220, v[228:229], off offset:3072 nt
	global_load_dword v221, v[228:229], off offset:3328 nt
	global_load_dword v222, v[228:229], off offset:3584 nt
	global_load_dword v223, v[228:229], off offset:3840 nt
	global_load_dword v224, v53, s[44:45]
	global_load_dword v225, v53, s[44:45] offset:4
	global_load_dword v226, v53, s[44:45] offset:8
	global_load_dword v227, v53, s[44:45] offset:12
	s_waitcnt vmcnt(0)
	s_branch .Lfin_copy

; #define GAS __attribute__((address_space(1)))
; __global__ void __launch_bounds__(NTHREADS, 2) fwd(Args args) {
;     ...
;         for (int t0 = 2 * gw; t0 < SEQ; t0 += 2 * NGW) {
;             unsigned long long hr[2][4]; unsigned pr[2][2][4]; int sl[2][2];
; #pragma unroll
;             for (int r = 0; r < 2; ++r) { const int t = t0 + r;
;                 const GAS unsigned long long* hp = (const GAS unsigned long long*)(HN + (size_t)t * DM) + F.lane;
; #pragma unroll
;                 for (int q = 0; q < 4; ++q) hr[r][q] = __builtin_nontemporal_load(hp + 64 * q);
; #pragma unroll
;                 for (int k = 0; k < 2; ++k) { const GAS unsigned* pa = (const GAS unsigned*)((const unsigned char*)PAIR + (size_t)(2 * t + k) * DM) + F.lane;
; #pragma unroll
;                     for (int q = 0; q < 4; ++q) pr[r][k][q] = __builtin_nontemporal_load(pa + 64 * q);
;                     sl[r][k] = SLOTOF[2 * t + k]; } }
.LBB0_1479:
	s_waitcnt vmcnt(8)
.Lfin_copy:
	v_mov_b32_e32 v16, v192
	v_mov_b32_e32 v17, v193
	v_mov_b32_e32 v18, v194
	v_mov_b32_e32 v19, v195
	v_mov_b32_e32 v20, v196
	v_mov_b32_e32 v21, v197
	v_mov_b32_e32 v22, v198
	v_mov_b32_e32 v23, v199
	v_mov_b32_e32 v66, v200
	v_mov_b32_e32 v67, v201
	v_mov_b32_e32 v64, v202
	v_mov_b32_e32 v65, v203
	v_mov_b32_e32 v62, v204
	v_mov_b32_e32 v63, v205
	v_mov_b32_e32 v60, v206
	v_mov_b32_e32 v61, v207
	v_mov_b32_e32 v188, v208
	v_mov_b32_e32 v189, v209
	v_mov_b32_e32 v190, v210
	v_mov_b32_e32 v191, v211
	v_mov_b32_e32 v95, v212
	v_mov_b32_e32 v94, v213
	v_mov_b32_e32 v93, v214
	v_mov_b32_e32 v92, v215
	v_mov_b32_e32 v91, v216
	v_mov_b32_e32 v90, v217
	v_mov_b32_e32 v89, v218
	v_mov_b32_e32 v88, v219
	v_mov_b32_e32 v87, v220
	v_mov_b32_e32 v86, v221
	v_mov_b32_e32 v85, v222
	v_mov_b32_e32 v84, v223
	v_mov_b32_e32 v26, v224
	v_mov_b32_e32 v27, v225
	v_mov_b32_e32 v28, v226
	v_mov_b32_e32 v29, v227
	s_add_i32 s44, s4, 0x2000
	s_ashr_i32 s45, s44, 31
	s_lshl_b64 s[46:47], s[44:45], 10
	s_lshl_b64 s[44:45], s[44:45], 2
	s_add_u32 s44, s7, s44
	s_addc_u32 s45, s20, s45
	v_lshl_add_u64 v[228:229], v[54:55], 0, s[46:47]
	v_lshl_add_u64 v[230:231], v[58:59], 0, s[10:11]
	global_load_dwordx2 v[192:193], v[230:231], off nt
	global_load_dwordx2 v[194:195], v[230:231], off offset:512 nt
	global_load_dwordx2 v[196:197], v[230:231], off offset:1024 nt
	global_load_dwordx2 v[198:199], v[230:231], off offset:1536 nt
	global_load_dwordx2 v[200:201], v[230:231], off offset:2048 nt
	global_load_dwordx2 v[202:203], v[230:231], off offset:2560 nt
	global_load_dwordx2 v[204:205], v[230:231], off offset:3072 nt
	global_load_dwordx2 v[206:207], v[230:231], off offset:3584 nt
	global_load_dword v208, v[228:229], off nt
	global_load_dword v209, v[228:229], off offset:256 nt
	global_load_dword v210, v[228:229], off offset:512 nt
	global_load_dword v211, v[228:229], off offset:768 nt
	global_load_dword v212, v[228:229], off offset:1024 nt
	global_load_dword v213, v[228:229], off offset:1280 nt
	global_load_dword v214, v[228:229], off offset:1536 nt
	global_load_dword v215, v[228:229], off offset:1792 nt
	global_load_dword v216, v[228:229], off offset:2048 nt
	global_load_dword v217, v[228:229], off offset:2304 nt
	global_load_dword v218, v[228:229], off offset:2560 nt
	global_load_dword v219, v[228:229], off offset:2816 nt
	global_load_dword v220, v[228:229], off offset:3072 nt
	global_load_dword v221, v[228:229], off offset:3328 nt
	global_load_dword v222, v[228:229], off offset:3584 nt
	global_load_dword v223, v[228:229], off offset:3840 nt
	global_load_dword v224, v53, s[44:45]
	global_load_dword v225, v53, s[44:45] offset:4
	global_load_dword v226, v53, s[44:45] offset:8
	global_load_dword v227, v53, s[44:45] offset:12
	s_ashr_i32 s5, s4, 31
	s_lshl_b64 s[42:43], s[4:5], 10
	s_lshl_b64 s[16:17], s[4:5], 2
	s_add_u32 s18, s7, s16
	s_addc_u32 s19, s20, s17
	s_add_i32 s0, s4, 1
	s_ashr_i32 s1, s0, 31
	s_lshl_b64 s[12:13], s[0:1], 10
	s_lshl_b64 s[0:1], s[0:1], 2
	s_add_u32 s34, s7, s0
	s_addc_u32 s35, s20, s1
	s_add_i32 s12, s4, 2
	s_ashr_i32 s13, s12, 31
	s_lshl_b64 s[14:15], s[12:13], 10
	s_lshl_b64 s[14:15], s[12:13], 2
	s_add_u32 s36, s7, s14
	s_addc_u32 s37, s20, s15
	s_add_i32 s12, s4, 3
	s_ashr_i32 s13, s12, 31
	s_lshl_b64 s[38:39], s[12:13], 10
	s_lshl_b64 s[12:13], s[12:13], 2
	s_add_u32 s38, s7, s12
	s_addc_u32 s39, s20, s13
	s_mov_b64 s[18:19], -1
	v_lshlrev_b32_e32 v52, 4, v162
	v_lshlrev_b32_e32 v44, 16, v16
	v_and_b32_e32 v45, 0xffff0000, v16
	v_alignbit_b32 v16, v17, v16, 16
	v_and_b32_e32 v47, 0xffff0000, v17
	v_lshlrev_b32_e32 v48, 16, v18
	v_and_b32_e32 v49, 0xffff0000, v18
	v_alignbit_b32 v17, v19, v18, 16
	v_and_b32_e32 v51, 0xffff0000, v19
	v_alignbit_b32 v18, v21, v20, 16
	v_alignbit_b32 v19, v23, v22, 16
	v_readfirstlane_b32 s37, v26
	s_ashr_i32 s2, s37, 8
	v_lshlrev_b32_e32 v70, 16, v20
	v_and_b32_e32 v71, 0xffff0000, v20
	v_and_b32_e32 v73, 0xffff0000, v21
	v_lshlrev_b32_e32 v68, 16, v22
	v_and_b32_e32 v69, 0xffff0000, v22
	v_and_b32_e32 v75, 0xffff0000, v23
	v_and_b32_e32 v46, 0xffff0000, v16
	v_and_b32_e32 v50, 0xffff0000, v17
	v_and_b32_e32 v72, 0xffff0000, v18
	v_and_b32_e32 v74, 0xffff0000, v19
	s_cmpk_gt_i32 s2, 0x7f
	v_readfirstlane_b32 s36, v27
	v_readfirstlane_b32 s35, v28
	v_readfirstlane_b32 s34, v29
	s_cbranch_scc0 .LBB0_1481
; #define GAS __attribute__((address_space(1)))
; __global__ void __launch_bounds__(NTHREADS, 2) fwd(Args args) {
;     ...
;                     } else { const int lt = (slot >> 8) - 128, rl = slot & 255; const float gt = GATES[2 * t + k] * (1.0f / 32.0f);
; #pragma unroll
;                         for (int q = 0; q < 4; ++q) { const GAS f32x4* pp = (const GAS f32x4*)(PART + (size_t)((lt * 4 + q) * 7) * 65536 + rl * 256) + F.lane; f32x4 s = pp[0];
; #pragma unroll
;                             for (int s7 = 1; s7 < 7; ++s7) s += pp[(size_t)s7 * 16384];
	s_add_u32 s38, s21, s16
	s_addc_u32 s39, s22, s17
	s_lshl_b32 s16, s37, 10
	s_and_b32 s16, s16, 0x3fc00
	s_add_u32 s16, s23, s16
	s_mul_i32 s18, s2, 28
	s_addc_u32 s17, s24, 0
	s_add_i32 s2, s18, 0xfffff200
	s_lshl_b64 s[40:41], s[2:3], 18
	s_add_u32 s40, s16, s40
	s_addc_u32 s41, s17, s41
	v_lshl_add_u64 v[36:37], s[40:41], 0, v[52:53]
	v_add_co_u32_e32 v28, vcc, s26, v36
	s_add_i32 s2, s18, 0xfffff207
	s_nop 0
	v_addc_co_u32_e32 v29, vcc, 0, v37, vcc
	v_add_co_u32_e32 v30, vcc, s27, v36
	global_load_dword v163, v53, s[38:39]
	global_load_dwordx4 v[16:19], v52, s[40:41]
	v_addc_co_u32_e32 v31, vcc, 0, v37, vcc
	v_add_co_u32_e32 v38, vcc, s28, v36
	s_lshl_b64 s[38:39], s[2:3], 18
	s_nop 0
	v_addc_co_u32_e32 v39, vcc, 0, v37, vcc
	v_add_co_u32_e32 v40, vcc, s29, v36
	s_add_u32 s38, s16, s38
	s_nop 0
	v_addc_co_u32_e32 v41, vcc, 0, v37, vcc
	v_add_co_u32_e32 v96, vcc, s30, v36
	s_addc_u32 s39, s17, s39
	s_nop 0
	v_addc_co_u32_e32 v97, vcc, 0, v37, vcc
	v_add_co_u32_e32 v98, vcc, s31, v36
	v_lshl_add_u64 v[112:113], s[38:39], 0, v[52:53]
	s_nop 0
	v_addc_co_u32_e32 v99, vcc, 0, v37, vcc
	v_add_co_u32_e32 v104, vcc, s26, v112
	s_add_i32 s2, s18, 0xfffff20e
	s_nop 0
	v_addc_co_u32_e32 v105, vcc, 0, v113, vcc
	v_add_co_u32_e32 v106, vcc, s27, v112
	s_lshl_b64 s[40:41], s[2:3], 18
	s_nop 0
	v_addc_co_u32_e32 v107, vcc, 0, v113, vcc
	v_add_co_u32_e32 v114, vcc, s28, v112
	s_add_u32 s40, s16, s40
	s_nop 0
	v_addc_co_u32_e32 v115, vcc, 0, v113, vcc
	v_add_co_u32_e32 v116, vcc, s29, v112
	s_addc_u32 s41, s17, s41
	s_nop 0
	v_addc_co_u32_e32 v117, vcc, 0, v113, vcc
	v_add_co_u32_e32 v120, vcc, s30, v112
	v_lshl_add_u64 v[144:145], s[40:41], 0, v[52:53]
	s_nop 0
	v_addc_co_u32_e32 v121, vcc, 0, v113, vcc
	v_add_co_u32_e32 v122, vcc, s31, v112
	s_add_i32 s2, s18, 0xfffff215
	s_nop 0
	v_addc_co_u32_e32 v123, vcc, 0, v113, vcc
	v_add_co_u32_e32 v128, vcc, s26, v144
	global_load_dwordx4 v[20:23], v[28:29], off
	global_load_dwordx4 v[24:27], v[30:31], off
	v_addc_co_u32_e32 v129, vcc, 0, v145, vcc
	v_add_co_u32_e32 v132, vcc, s27, v144
	global_load_dwordx4 v[28:31], v[38:39], off
	global_load_dwordx4 v[32:35], v[40:41], off
	v_addc_co_u32_e32 v133, vcc, 0, v145, vcc
	v_add_co_u32_e32 v136, vcc, s28, v144
	global_load_dwordx4 v[36:39], v[96:97], off
	global_load_dwordx4 v[40:43], v[98:99], off
	v_addc_co_u32_e32 v137, vcc, 0, v145, vcc
	v_add_co_u32_e32 v140, vcc, s29, v144
	global_load_dwordx4 v[96:99], v[104:105], off
	global_load_dwordx4 v[100:103], v[106:107], off
	v_addc_co_u32_e32 v141, vcc, 0, v145, vcc
	global_load_dwordx4 v[104:107], v[114:115], off
	global_load_dwordx4 v[108:111], v[116:117], off
	s_nop 0
	global_load_dwordx4 v[112:115], v[120:121], off
	global_load_dwordx4 v[116:119], v[122:123], off
	s_nop 0
	global_load_dwordx4 v[120:123], v52, s[38:39]
	global_load_dwordx4 v[124:127], v52, s[40:41]
	v_add_co_u32_e32 v146, vcc, s30, v144
	s_lshl_b64 s[18:19], s[2:3], 18
	s_waitcnt lgkmcnt(0)
	v_addc_co_u32_e32 v147, vcc, 0, v145, vcc
	s_add_u32 s16, s16, s18
	v_add_co_u32_e32 v148, vcc, s31, v144
	s_addc_u32 s17, s17, s19
	s_nop 0
	v_addc_co_u32_e32 v149, vcc, 0, v145, vcc
	v_lshl_add_u64 v[160:161], s[16:17], 0, v[52:53]
	v_add_co_u32_e32 v156, vcc, s26, v160
	global_load_dwordx4 v[128:131], v[128:129], off
	s_nop 0
	global_load_dwordx4 v[132:135], v[132:133], off
	v_addc_co_u32_e32 v157, vcc, 0, v161, vcc
	v_add_co_u32_e32 v164, vcc, s27, v160
	global_load_dwordx4 v[136:139], v[136:137], off
	s_nop 0
	global_load_dwordx4 v[140:143], v[140:141], off
	v_addc_co_u32_e32 v165, vcc, 0, v161, vcc
	v_add_co_u32_e32 v168, vcc, s28, v160
	global_load_dwordx4 v[144:147], v[146:147], off
	s_nop 0
	global_load_dwordx4 v[148:151], v[148:149], off
	v_addc_co_u32_e32 v169, vcc, 0, v161, vcc
	v_add_co_u32_e32 v172, vcc, s29, v160
	global_load_dwordx4 v[152:155], v52, s[16:17]
	s_nop 0
	v_addc_co_u32_e32 v173, vcc, 0, v161, vcc
	global_load_dwordx4 v[156:159], v[156:157], off
	s_nop 0
	global_load_dwordx4 v[164:167], v[164:165], off
	v_add_co_u32_e32 v176, vcc, s30, v160
	global_load_dwordx4 v[168:171], v[168:169], off
	s_nop 0
	global_load_dwordx4 v[172:175], v[172:173], off
	v_addc_co_u32_e32 v177, vcc, 0, v161, vcc
	v_add_co_u32_e32 v160, vcc, 0x180000, v160
	global_load_dwordx4 v[176:179], v[176:177], off
	s_nop 0
	v_addc_co_u32_e32 v161, vcc, 0, v161, vcc
	global_load_dwordx4 v[180:183], v[160:161], off
	s_waitcnt vmcnt(28)
; #define GAS __attribute__((address_space(1)))
; __global__ void __launch_bounds__(NTHREADS, 2) fwd(Args args) {
;     ...
;                     } else { const int lt = (slot >> 8) - 128, rl = slot & 255; const float gt = GATES[2 * t + k] * (1.0f / 32.0f);
; #pragma unroll
;                         for (int q = 0; q < 4; ++q) { const GAS f32x4* pp = (const GAS f32x4*)(PART + (size_t)((lt * 4 + q) * 7) * 65536 + rl * 256) + F.lane; f32x4 s = pp[0];
; #pragma unroll
;                             for (int s7 = 1; s7 < 7; ++s7) s += pp[(size_t)s7 * 16384];
;                             v[q] += s * gt; } } }
	v_mul_f32_e32 v160, 0x3d000000, v163
	s_waitcnt vmcnt(26)
	v_pk_add_f32 v[18:19], v[18:19], v[22:23]
	v_pk_add_f32 v[16:17], v[16:17], v[20:21]
	s_waitcnt vmcnt(25)
	v_pk_add_f32 v[18:19], v[18:19], v[26:27]
	v_pk_add_f32 v[16:17], v[16:17], v[24:25]
	s_waitcnt vmcnt(24)
	v_pk_add_f32 v[18:19], v[18:19], v[30:31]
	v_pk_add_f32 v[16:17], v[16:17], v[28:29]
	s_waitcnt vmcnt(23)
	v_pk_add_f32 v[18:19], v[18:19], v[34:35]
	v_pk_add_f32 v[16:17], v[16:17], v[32:33]
	s_waitcnt vmcnt(22)
	v_pk_add_f32 v[18:19], v[18:19], v[38:39]
	v_pk_add_f32 v[16:17], v[16:17], v[36:37]
	s_waitcnt vmcnt(21)
	v_pk_add_f32 v[18:19], v[18:19], v[42:43]
	v_pk_add_f32 v[16:17], v[16:17], v[40:41]
	v_pk_fma_f32 v[18:19], v[160:161], v[18:19], v[46:47] op_sel_hi:[0,1,1]
	v_pk_fma_f32 v[16:17], v[160:161], v[16:17], v[44:45] op_sel_hi:[0,1,1]
	s_waitcnt vmcnt(14)
	v_pk_add_f32 v[20:21], v[122:123], v[98:99]
	v_pk_add_f32 v[22:23], v[120:121], v[96:97]
	v_pk_add_f32 v[20:21], v[20:21], v[102:103]
	v_pk_add_f32 v[22:23], v[22:23], v[100:101]
	v_pk_add_f32 v[20:21], v[20:21], v[106:107]
	v_pk_add_f32 v[22:23], v[22:23], v[104:105]
	v_pk_add_f32 v[20:21], v[20:21], v[110:111]
	v_pk_add_f32 v[22:23], v[22:23], v[108:109]
	v_pk_add_f32 v[20:21], v[20:21], v[114:115]
	v_pk_add_f32 v[22:23], v[22:23], v[112:113]
	v_pk_add_f32 v[20:21], v[20:21], v[118:119]
	v_pk_add_f32 v[24:25], v[22:23], v[116:117]
	v_pk_fma_f32 v[22:23], v[160:161], v[20:21], v[50:51] op_sel_hi:[0,1,1]
	v_pk_fma_f32 v[20:21], v[160:161], v[24:25], v[48:49] op_sel_hi:[0,1,1]
	s_waitcnt vmcnt(12)
	v_pk_add_f32 v[24:25], v[126:127], v[130:131]
	v_pk_add_f32 v[26:27], v[124:125], v[128:129]
	s_waitcnt vmcnt(11)
	v_pk_add_f32 v[24:25], v[24:25], v[134:135]
	v_pk_add_f32 v[26:27], v[26:27], v[132:133]
	s_waitcnt vmcnt(10)
	v_pk_add_f32 v[24:25], v[24:25], v[138:139]
	v_pk_add_f32 v[26:27], v[26:27], v[136:137]
	s_waitcnt vmcnt(9)
	v_pk_add_f32 v[24:25], v[24:25], v[142:143]
	v_pk_add_f32 v[26:27], v[26:27], v[140:141]
	s_waitcnt vmcnt(8)
	v_pk_add_f32 v[24:25], v[24:25], v[146:147]
	v_pk_add_f32 v[26:27], v[26:27], v[144:145]
	s_waitcnt vmcnt(7)
	v_pk_add_f32 v[24:25], v[24:25], v[150:151]
	v_pk_add_f32 v[28:29], v[26:27], v[148:149]
	v_pk_fma_f32 v[26:27], v[160:161], v[24:25], v[72:73] op_sel_hi:[0,1,1]
	v_pk_fma_f32 v[24:25], v[160:161], v[28:29], v[70:71] op_sel_hi:[0,1,1]
	s_waitcnt vmcnt(5)
	v_pk_add_f32 v[28:29], v[154:155], v[158:159]
	v_pk_add_f32 v[30:31], v[152:153], v[156:157]
	s_waitcnt vmcnt(4)
	v_pk_add_f32 v[28:29], v[28:29], v[166:167]
	v_pk_add_f32 v[30:31], v[30:31], v[164:165]
	s_waitcnt vmcnt(3)
	v_pk_add_f32 v[28:29], v[28:29], v[170:171]
	v_pk_add_f32 v[30:31], v[30:31], v[168:169]
	s_waitcnt vmcnt(2)
	v_pk_add_f32 v[28:29], v[28:29], v[174:175]
	v_pk_add_f32 v[30:31], v[30:31], v[172:173]
	s_waitcnt vmcnt(1)
	v_pk_add_f32 v[28:29], v[28:29], v[178:179]
	v_pk_add_f32 v[30:31], v[30:31], v[176:177]
	s_waitcnt vmcnt(0)
	v_pk_add_f32 v[28:29], v[28:29], v[182:183]
	v_pk_add_f32 v[32:33], v[30:31], v[180:181]
	v_pk_fma_f32 v[30:31], v[160:161], v[28:29], v[74:75] op_sel_hi:[0,1,1]
	v_pk_fma_f32 v[28:29], v[160:161], v[32:33], v[68:69] op_sel_hi:[0,1,1]
	s_cbranch_execnz .LBB0_1483
	s_branch .LBB0_1482

; __global__ void __launch_bounds__(NTHREADS, 2) fwd(Args args) {
;     ...
;                 for (int k = 0; k < 2; ++k) { const int slot = sl[r][k];
;                     if ((slot >> 8) < 128) {
; #pragma unroll
;                         for (int q = 0; q < 4; ++q) { const unsigned a = pr[r][k][q];
;                             const auto lo = __builtin_amdgcn_cvt_pk_f32_fp8((int)a, false), hi = __builtin_amdgcn_cvt_pk_f32_fp8((int)a, true);
;                             v[q].x += lo[0] * 0.0625f; v[q].y += lo[1] * 0.0625f; v[q].z += hi[0] * 0.0625f; v[q].w += hi[1] * 0.0625f; }
.LBB0_1494:
	v_cvt_pk_f32_fp8_e32 v[32:33], v87
	v_cvt_pk_f32_fp8_sdwa v[36:37], v87 src0_sel:WORD_1
	v_cvt_pk_f32_fp8_e32 v[38:39], v86
	v_cvt_pk_f32_fp8_sdwa v[40:41], v86 src0_sel:WORD_1
	v_pk_fma_f32 v[34:35], v[32:33], s[6:7], v[16:17] op_sel_hi:[1,0,1]
	v_pk_fma_f32 v[32:33], v[36:37], s[6:7], v[18:19] op_sel_hi:[1,0,1]
	v_pk_fma_f32 v[38:39], v[38:39], s[6:7], v[20:21] op_sel_hi:[1,0,1]
	v_pk_fma_f32 v[36:37], v[40:41], s[6:7], v[22:23] op_sel_hi:[1,0,1]
	v_cvt_pk_f32_fp8_e32 v[16:17], v85
	v_cvt_pk_f32_fp8_sdwa v[18:19], v85 src0_sel:WORD_1
	v_cvt_pk_f32_fp8_e32 v[20:21], v84
	v_cvt_pk_f32_fp8_sdwa v[22:23], v84 src0_sel:WORD_1
	v_pk_fma_f32 v[42:43], v[16:17], s[6:7], v[24:25] op_sel_hi:[1,0,1]
	v_pk_fma_f32 v[40:41], v[18:19], s[6:7], v[26:27] op_sel_hi:[1,0,1]
	v_pk_fma_f32 v[46:47], v[20:21], s[6:7], v[28:29] op_sel_hi:[1,0,1]
	v_pk_fma_f32 v[44:45], v[22:23], s[6:7], v[30:31] op_sel_hi:[1,0,1]
	s_branch .LBB0_1478
.LBB0_1495:
	s_waitcnt vmcnt(0)
	s_endpgm
